# block forward substitution unrolled with hoisted loads on top of stage 1b rewrite
# baseline (speedup 1.0000x reference)
.LBB0_434:
	s_or_b64 exec, exec, s[0:1]
	v_or_b32_e32 v0, s67, v51
	v_lshrrev_b32_e32 v12, 4, v49
	v_mul_u32_u24_e32 v2, 0x90, v0
	v_lshlrev_b32_e32 v14, 3, v12
	v_add3_u32 v15, v132, v2, v44
	v_lshrrev_b32_e32 v2, 2, v51
	v_mov_b32_e32 v3, s2
	s_movk_i32 s0, 0x240
	v_and_b32_e32 v17, 3, v103
	v_mad_u32_u24 v3, v12, s0, v3
	v_mul_u32_u24_e32 v2, 0x90, v2
	v_lshlrev_b32_e32 v17, 3, v17
	v_mad_u32_u24 v18, v0, s39, v14
	v_mul_u32_u24_e32 v0, 48, v51
	s_mov_b32 s0, 0x1dd00
	v_mul_u32_u24_e32 v7, 0x90, v10
	v_mul_u32_u24_e32 v5, 0x90, v8
	v_or_b32_e32 v16, 32, v14
	v_add3_u32 v17, v3, v2, v17
	v_add3_u32 v19, v0, v14, s0
	v_mad_u32_u24 v20, v51, s39, v1
	s_mov_b32 s8, 0
	s_waitcnt lgkmcnt(0)
	s_barrier
	v_add_u32_e32 v245, v111, v20
	v_add_u32_e32 v207, v111, v19
	v_add_u32_e32 v24, v132, v18
	v_mov_b32_e32 v230, v15
	s_and_b64 vcc, exec, s[68:69]
	v_add_u32_e32 v245, 0x12000, v245
	s_cbranch_vccz .Lsub_w03
	v_add_u32_e32 v197, v111, v18
	v_add_u32_e32 v197, 0x14400, v197
	ds_read_b64 v[208:209], v197
	ds_read_b64 v[210:211], v197 offset:32
	ds_read_b64 v[228:229], v197 offset:64
	ds_read_b64 v[250:251], v197 offset:96
	s_branch .Lsub_rhs
.Lsub_w03:
	v_add_u32_e32 v197, v111, v17
	ds_read_b64_tr_b16 v[208:209], v197
	ds_read_b64_tr_b16 v[210:211], v197 offset:2304
	ds_read_b64_tr_b16 v[228:229], v197 offset:4608
	ds_read_b64_tr_b16 v[250:251], v197 offset:6912
.Lsub_rhs:
	ds_read_b64 v[0:1], v207
	ds_read_b128 v[224:227], v245 offset:2304
	ds_read_b128 v[246:249], v245 offset:4608
	ds_read_b128 v[216:219], v245 offset:6912
	ds_read_b128 v[220:223], v245 offset:6976
	v_mov_b32_e32 v2, v105
	v_mov_b32_e32 v3, v105
	v_mov_b32_e32 v104, v105
	v_cmp_gt_u32_e32 vcc, 16, v14
	s_waitcnt lgkmcnt(0)
	v_mov_b32_e32 v102, v208
	v_mov_b32_e32 v103, v209
	s_nop 1
	v_mfma_f32_16x16x32_bf16 v[26:29], v[0:3], v[102:105], 0
	ds_read_b64 v[0:1], v207 offset:768
	v_lshlrev_b32_e32 v18, 16, v210
	v_and_b32_e32 v19, 0xffff0000, v210
	v_lshlrev_b32_e32 v20, 16, v211
	v_and_b32_e32 v21, 0xffff0000, v211
	v_cndmask_b32_e32 v224, 0, v224, vcc
	v_cndmask_b32_e32 v225, 0, v225, vcc
	v_cndmask_b32_e32 v226, 0, v226, vcc
	v_cndmask_b32_e32 v227, 0, v227, vcc
	v_cvt_pk_bf16_f32 v22, v26, v27
	v_cvt_pk_bf16_f32 v23, v28, v29
	ds_write_b64 v24, v[22:23]
	ds_read_b128 v[14:17], v230
	s_waitcnt lgkmcnt(0)
	v_mfma_f32_16x16x32_bf16 v[18:21], v[224:227], v[14:17], v[18:21]
	v_cndmask_b32_e32 v220, 0, v220, vcc
	v_cndmask_b32_e32 v221, 0, v221, vcc
	v_cndmask_b32_e32 v222, 0, v222, vcc
	v_cndmask_b32_e32 v223, 0, v223, vcc
	s_nop 3
	v_cvt_pk_bf16_f32 v102, v18, v19
	v_cvt_pk_bf16_f32 v103, v20, v21
	s_nop 1
	v_mfma_f32_16x16x32_bf16 v[26:29], v[0:3], v[102:105], 0
	ds_read_b64 v[0:1], v207 offset:1536
	v_lshlrev_b32_e32 v18, 16, v228
	v_and_b32_e32 v19, 0xffff0000, v228
	v_lshlrev_b32_e32 v20, 16, v229
	v_and_b32_e32 v21, 0xffff0000, v229
	s_nop 3
	v_cvt_pk_bf16_f32 v22, v26, v27
	v_cvt_pk_bf16_f32 v23, v28, v29
	ds_write_b64 v24, v[22:23] offset:32
	ds_read_b128 v[14:17], v230
	s_waitcnt lgkmcnt(0)
	v_mfma_f32_16x16x32_bf16 v[18:21], v[246:249], v[14:17], v[18:21]
	s_nop 7
	v_cvt_pk_bf16_f32 v102, v18, v19
	v_cvt_pk_bf16_f32 v103, v20, v21
	s_nop 1
	v_mfma_f32_16x16x32_bf16 v[26:29], v[0:3], v[102:105], 0
	ds_read_b64 v[0:1], v207 offset:2304
	v_lshlrev_b32_e32 v18, 16, v250
	v_and_b32_e32 v19, 0xffff0000, v250
	v_lshlrev_b32_e32 v20, 16, v251
	v_and_b32_e32 v21, 0xffff0000, v251
	s_nop 3
	v_cvt_pk_bf16_f32 v22, v26, v27
	v_cvt_pk_bf16_f32 v23, v28, v29
	ds_write_b64 v24, v[22:23] offset:64
	ds_read_b128 v[14:17], v230
	ds_read_b128 v[224:227], v230 offset:64
	s_waitcnt lgkmcnt(0)
	v_mfma_f32_16x16x32_bf16 v[18:21], v[216:219], v[14:17], v[18:21]
	v_mfma_f32_16x16x32_bf16 v[18:21], v[220:223], v[224:227], v[18:21]
	s_nop 7
	v_cvt_pk_bf16_f32 v102, v18, v19
	v_cvt_pk_bf16_f32 v103, v20, v21
	s_nop 1
	v_mfma_f32_16x16x32_bf16 v[26:29], v[0:3], v[102:105], 0
	s_nop 7
	v_cvt_pk_bf16_f32 v22, v26, v27
	v_cvt_pk_bf16_f32 v23, v28, v29
	ds_write_b64 v24, v[22:23] offset:96
	s_branch .LBB0_380
